# speedup vs baseline: 1.0291x; 1.0291x over previous
_Z2kBPKfPKDv4_jPKDF16_S0_S0_S0_Pf:
	v_lshrrev_b32_e32 v11, 7, v0
	s_load_dwordx8 s[4:11], s[0:1], 0x0
	v_lshl_or_b32 v2, s2, 2, v11
	s_mov_b32 s2, 0x4ec4ec4f
	v_mul_hi_i32 v1, v2, s2
	v_lshrrev_b32_e32 v3, 31, v1
	v_ashrrev_i32_e32 v1, 2, v1
	v_add_u32_e32 v1, v1, v3
	v_and_b32_e32 v108, 15, v0
	v_mad_u64_u32 v[4:5], s[2:3], v1, -13, v[2:3]
	v_lshlrev_b32_e32 v102, 4, v0
	v_mov_b32_e32 v103, 0
	v_lshl_or_b32 v10, v4, 4, v108
	s_waitcnt lgkmcnt(0)
	v_lshl_add_u64 v[4:5], s[8:9], 0, v[102:103]
	s_movk_i32 s2, 0x2000
	v_add_co_u32_e32 v6, vcc, s2, v4
	s_movk_i32 s2, 0x4000
	s_nop 0
	v_addc_co_u32_e32 v7, vcc, 0, v5, vcc
	v_add_co_u32_e32 v8, vcc, s2, v4
	s_movk_i32 s2, 0x6000
	s_nop 0
	v_addc_co_u32_e32 v9, vcc, 0, v5, vcc
	global_load_dwordx4 v[14:17], v102, s[8:9]
	global_load_dwordx4 v[18:21], v[6:7], off
	global_load_dwordx4 v[22:25], v[8:9], off
	v_add_co_u32_e32 v6, vcc, s2, v4
	s_mov_b32 s2, 0x8000
	s_nop 0
	v_addc_co_u32_e32 v7, vcc, 0, v5, vcc
	v_add_co_u32_e32 v8, vcc, s2, v4
	s_mov_b32 s2, 0xa000
	s_nop 0
	v_addc_co_u32_e32 v9, vcc, 0, v5, vcc
	global_load_dwordx4 v[26:29], v[6:7], off
	global_load_dwordx4 v[30:33], v[8:9], off
	v_add_co_u32_e32 v6, vcc, s2, v4
	s_mov_b32 s2, 0xc000
	s_nop 0
	v_addc_co_u32_e32 v7, vcc, 0, v5, vcc
	v_add_co_u32_e32 v8, vcc, s2, v4
	s_mov_b32 s2, 0xe000
	s_nop 0
	v_addc_co_u32_e32 v9, vcc, 0, v5, vcc
	v_add_co_u32_e32 v4, vcc, s2, v4
	s_movk_i32 s2, 0xc8
	s_nop 0
	v_addc_co_u32_e32 v5, vcc, 0, v5, vcc
	global_load_dwordx4 v[34:37], v[6:7], off
	global_load_dwordx4 v[38:41], v[8:9], off
	v_mov_b32_e32 v3, 0xc7
	v_cmp_gt_i32_e32 vcc, s2, v10
	global_load_dwordx4 v[42:45], v[4:5], off
	s_movk_i32 s2, 0x320
	v_cndmask_b32_e32 v4, v3, v10, vcc
	v_mad_u64_u32 v[4:5], s[2:3], v1, s2, v[4:5]
	v_and_b32_e32 v6, 48, v0
	v_mov_b32_e32 v7, v103
	v_ashrrev_i32_e32 v5, 31, v4
	v_lshl_add_u64 v[8:9], s[4:5], 0, v[6:7]
	v_lshlrev_b64 v[12:13], 6, v[4:5]
	v_lshl_add_u64 v[12:13], v[8:9], 0, v[12:13]
	global_load_dwordx4 v[46:49], v[12:13], off nt
	v_add_u32_e32 v12, 0xc8, v4
	v_ashrrev_i32_e32 v13, 31, v12
	v_lshlrev_b64 v[12:13], 6, v[12:13]
	v_lshl_add_u64 v[12:13], v[8:9], 0, v[12:13]
	global_load_dwordx4 v[50:53], v[12:13], off nt
	v_add_u32_e32 v12, 0x190, v4
	v_ashrrev_i32_e32 v13, 31, v12
	v_lshlrev_b64 v[12:13], 6, v[12:13]
	v_lshl_add_u64 v[12:13], v[8:9], 0, v[12:13]
	global_load_dwordx4 v[54:57], v[12:13], off nt
	v_add_u32_e32 v4, 0x258, v4
	v_ashrrev_i32_e32 v5, 31, v4
	v_lshlrev_b64 v[4:5], 6, v[4:5]
	v_lshl_add_u64 v[4:5], v[8:9], 0, v[4:5]
	global_load_dwordx4 v[58:61], v[4:5], off nt
	v_and_b32_e32 v13, 63, v0
	v_lshl_or_b32 v2, v2, 8, v13
	v_ashrrev_i32_e32 v3, 31, v2
	v_lshl_add_u64 v[2:3], v[2:3], 4, s[6:7]
	global_load_dwordx4 v[62:65], v[2:3], off nt
	global_load_dwordx4 v[66:69], v[2:3], off offset:1024 nt
	global_load_dwordx4 v[70:73], v[2:3], off offset:2048 nt
	global_load_dwordx4 v[74:77], v[2:3], off offset:3072 nt
	s_load_dwordx4 s[4:7], s[0:1], 0x20
	v_bfe_u32 v12, v0, 6, 1
	v_lshl_add_u64 v[2:3], s[10:11], 0, v[6:7]
	v_and_b32_e32 v0, 64, v0
	v_cmp_gt_u32_e64 s[2:3], 16, v13
	s_waitcnt lgkmcnt(0)
	v_lshl_add_u64 v[4:5], s[4:5], 0, v[6:7]
	v_lshlrev_b32_e32 v6, 8, v12
	v_lshl_add_u64 v[104:105], v[2:3], 0, v[6:7]
	v_lshl_add_u64 v[106:107], v[4:5], 0, v[6:7]
	global_load_dwordx4 v[78:81], v[104:105], off
	global_load_dwordx4 v[82:85], v[104:105], off offset:64
	global_load_dwordx4 v[86:89], v[106:107], off
	global_load_dwordx4 v[90:93], v[106:107], off offset:64
	global_load_dwordx4 v[94:97], v[104:105], off offset:128
	global_load_dwordx4 v[6:9], v[104:105], off offset:192
	global_load_dwordx4 v[98:101], v[106:107], off offset:128
	global_load_dwordx4 v[2:5], v[106:107], off offset:192
	s_load_dword s6, s[6:7], 0x0
	s_waitcnt vmcnt(23)
	ds_write_b128 v102, v[14:17]
	s_waitcnt vmcnt(22)
	ds_write_b128 v102, v[18:21] offset:8192
	s_waitcnt vmcnt(21)
	ds_write_b128 v102, v[22:25] offset:16384
	s_waitcnt vmcnt(20)
	ds_write_b128 v102, v[26:29] offset:24576
	s_waitcnt vmcnt(19)
	ds_write_b128 v102, v[30:33] offset:32768
	s_waitcnt vmcnt(18)
	ds_write_b128 v102, v[34:37] offset:40960
	s_waitcnt vmcnt(17)
	ds_write_b128 v102, v[38:41] offset:49152
	s_waitcnt vmcnt(16)
	ds_write_b128 v102, v[42:45] offset:57344
	v_lshlrev_b32_e32 v14, 15, v12
	v_lshl_or_b32 v38, v13, 4, v14
	s_waitcnt lgkmcnt(0)
	s_barrier
	ds_read_b128 v[14:17], v38
	ds_read_b128 v[18:21], v38 offset:1024
	s_waitcnt vmcnt(15) lgkmcnt(1)
	v_mfma_f32_16x16x32_f16 v[14:17], v[14:17], v[46:49], 0
	ds_read_b128 v[22:25], v38 offset:2048
	ds_read_b128 v[26:29], v38 offset:10240
	ds_read_b128 v[30:33], v38 offset:18432
	s_waitcnt vmcnt(14) lgkmcnt(3)
	v_mfma_f32_16x16x32_f16 v[14:17], v[18:21], v[50:53], v[14:17]
	ds_read_b128 v[18:21], v38 offset:3072
	ds_read_b128 v[34:37], v38 offset:26624
	v_cmp_ne_u32_e64 s[4:5], 0, v0
	s_waitcnt vmcnt(13) lgkmcnt(4)
	v_mfma_f32_16x16x32_f16 v[14:17], v[22:25], v[54:57], v[14:17]
	ds_read_b128 v[22:25], v38 offset:4096
	s_and_b64 s[8:9], s[4:5], s[2:3]
	v_lshlrev_b32_e32 v0, 2, v108
	s_waitcnt vmcnt(12) lgkmcnt(2)
	v_mfma_f32_16x16x32_f16 v[14:17], v[18:21], v[58:61], v[14:17]
	ds_read_b128 v[18:21], v38 offset:5120
	s_waitcnt vmcnt(11) lgkmcnt(1)
	v_mfma_f32_16x16x32_f16 v[14:17], v[22:25], v[62:65], v[14:17]
	ds_read_b128 v[22:25], v38 offset:6144
	s_waitcnt vmcnt(10) lgkmcnt(1)
	v_mfma_f32_16x16x32_f16 v[14:17], v[18:21], v[66:69], v[14:17]
	ds_read_b128 v[18:21], v38 offset:7168
	s_waitcnt vmcnt(9) lgkmcnt(1)
	v_mfma_f32_16x16x32_f16 v[14:17], v[22:25], v[70:73], v[14:17]
	ds_read_b128 v[22:25], v38 offset:8192
	s_waitcnt vmcnt(8) lgkmcnt(1)
	v_mfma_f32_16x16x32_f16 v[14:17], v[18:21], v[74:77], v[14:17]
	ds_read_b128 v[18:21], v38 offset:9216
	s_waitcnt lgkmcnt(1)
	v_mfma_f32_16x16x32_f16 v[22:25], v[22:25], v[46:49], 0
	s_waitcnt vmcnt(7)
	s_nop 3
	v_add_f32_e32 v14, v14, v78
	v_mul_f32_e32 v14, 0x4038aa3b, v14
	v_add_f32_e32 v15, v15, v79
	s_waitcnt lgkmcnt(0)
	v_mfma_f32_16x16x32_f16 v[18:21], v[18:21], v[50:53], v[22:25]
	v_exp_f32_e32 v14, v14
	v_mul_f32_e32 v15, 0x4038aa3b, v15
	s_nop 0
	ds_read_b128 v[22:25], v38 offset:11264
	v_mfma_f32_16x16x32_f16 v[18:21], v[26:29], v[54:57], v[18:21]
	ds_read_b128 v[26:29], v38 offset:12288
	v_add_f32_e32 v16, v16, v80
	v_exp_f32_e32 v15, v15
	s_waitcnt lgkmcnt(1)
	v_mfma_f32_16x16x32_f16 v[18:21], v[22:25], v[58:61], v[18:21]
	ds_read_b128 v[22:25], v38 offset:13312
	v_mul_f32_e32 v16, 0x4038aa3b, v16
	v_add_f32_e32 v17, v17, v81
	s_waitcnt lgkmcnt(1)
	v_mfma_f32_16x16x32_f16 v[18:21], v[26:29], v[62:65], v[18:21]
	ds_read_b128 v[26:29], v38 offset:14336
	v_exp_f32_e32 v16, v16
	v_mul_f32_e32 v17, 0x4038aa3b, v17
	s_waitcnt lgkmcnt(1)
	v_mfma_f32_16x16x32_f16 v[18:21], v[22:25], v[66:69], v[18:21]
	ds_read_b128 v[22:25], v38 offset:15360
	v_exp_f32_e32 v17, v17
	v_add_f32_e32 v14, 1.0, v14
	s_waitcnt lgkmcnt(1)
	v_mfma_f32_16x16x32_f16 v[18:21], v[26:29], v[70:73], v[18:21]
	ds_read_b128 v[26:29], v38 offset:16384
	v_rcp_f32_e32 v14, v14
	v_add_f32_e32 v15, 1.0, v15
	s_waitcnt lgkmcnt(1)
	v_mfma_f32_16x16x32_f16 v[18:21], v[22:25], v[74:77], v[18:21]
	ds_read_b128 v[22:25], v38 offset:17408
	v_rcp_f32_e32 v15, v15
	v_add_f32_e32 v16, 1.0, v16
	s_waitcnt lgkmcnt(1)
	v_mfma_f32_16x16x32_f16 v[26:29], v[26:29], v[46:49], 0
	v_rcp_f32_e32 v16, v16
	v_add_f32_e32 v17, 1.0, v17
	v_rcp_f32_e32 v17, v17
	s_waitcnt lgkmcnt(0)
	v_mfma_f32_16x16x32_f16 v[22:25], v[22:25], v[50:53], v[26:29]
	v_fma_f32 v14, v14, -2.0, 1.0
	s_nop 1
	ds_read_b128 v[26:29], v38 offset:19456
	s_waitcnt vmcnt(5)
	v_fma_f32 v14, v14, v86, 0
	v_mfma_f32_16x16x32_f16 v[22:25], v[30:33], v[54:57], v[22:25]
	ds_read_b128 v[30:33], v38 offset:20480
	v_fma_f32 v15, v15, -2.0, 1.0
	v_fmac_f32_e32 v14, v15, v87
	s_waitcnt lgkmcnt(1)
	v_mfma_f32_16x16x32_f16 v[22:25], v[26:29], v[58:61], v[22:25]
	ds_read_b128 v[26:29], v38 offset:21504
	v_fma_f32 v15, v16, -2.0, 1.0
	v_fmac_f32_e32 v14, v15, v88
	s_waitcnt lgkmcnt(1)
	v_mfma_f32_16x16x32_f16 v[22:25], v[30:33], v[62:65], v[22:25]
	ds_read_b128 v[30:33], v38 offset:22528
	v_fma_f32 v15, v17, -2.0, 1.0
	v_add_f32_e32 v16, v18, v82
	s_waitcnt lgkmcnt(1)
	v_mfma_f32_16x16x32_f16 v[22:25], v[26:29], v[66:69], v[22:25]
	ds_read_b128 v[26:29], v38 offset:23552
	v_add_f32_e32 v17, v19, v83
	v_mul_f32_e32 v16, 0x4038aa3b, v16
	s_waitcnt lgkmcnt(1)
	v_mfma_f32_16x16x32_f16 v[22:25], v[30:33], v[70:73], v[22:25]
	ds_read_b128 v[30:33], v38 offset:24576
	v_mul_f32_e32 v17, 0x4038aa3b, v17
	v_exp_f32_e32 v16, v16
	s_waitcnt lgkmcnt(1)
	v_mfma_f32_16x16x32_f16 v[22:25], v[26:29], v[74:77], v[22:25]
	ds_read_b128 v[26:29], v38 offset:25600
	v_exp_f32_e32 v17, v17
	v_fmac_f32_e32 v14, v15, v89
	s_waitcnt lgkmcnt(1)
	v_mfma_f32_16x16x32_f16 v[30:33], v[30:33], v[46:49], 0
	v_add_f32_e32 v15, 1.0, v16
	v_add_f32_e32 v16, 1.0, v17
	v_add_f32_e32 v17, v20, v84
	s_waitcnt lgkmcnt(0)
	v_mfma_f32_16x16x32_f16 v[26:29], v[26:29], v[50:53], v[30:33]
	v_rcp_f32_e32 v15, v15
	s_nop 1
	ds_read_b128 v[30:33], v38 offset:27648
	v_mul_f32_e32 v17, 0x4038aa3b, v17
	v_mfma_f32_16x16x32_f16 v[26:29], v[34:37], v[54:57], v[26:29]
	ds_read_b128 v[34:37], v38 offset:28672
	v_rcp_f32_e32 v16, v16
	v_exp_f32_e32 v17, v17
	s_waitcnt lgkmcnt(1)
	v_mfma_f32_16x16x32_f16 v[26:29], v[30:33], v[58:61], v[26:29]
	ds_read_b128 v[30:33], v38 offset:29696
	v_fma_f32 v15, v15, -2.0, 1.0
	s_waitcnt vmcnt(4)
	v_fmac_f32_e32 v14, v15, v90
	v_fma_f32 v15, v16, -2.0, 1.0
	v_add_f32_e32 v16, 1.0, v17
	v_add_f32_e32 v17, v21, v85
	s_waitcnt lgkmcnt(1)
	v_mfma_f32_16x16x32_f16 v[26:29], v[34:37], v[62:65], v[26:29]
	ds_read_b128 v[34:37], v38 offset:30720
	v_rcp_f32_e32 v16, v16
	v_mul_f32_e32 v17, 0x4038aa3b, v17
	v_exp_f32_e32 v17, v17
	s_waitcnt lgkmcnt(1)
	v_mfma_f32_16x16x32_f16 v[26:29], v[30:33], v[66:69], v[26:29]
	ds_read_b128 v[30:33], v38 offset:31744
	v_fmac_f32_e32 v14, v15, v91
	v_fma_f32 v15, v16, -2.0, 1.0
	s_waitcnt vmcnt(3)
	v_add_f32_e32 v16, v22, v94
	v_fmac_f32_e32 v14, v15, v92
	v_add_f32_e32 v15, 1.0, v17
	v_mul_f32_e32 v16, 0x4038aa3b, v16
	v_add_f32_e32 v17, v23, v95
	v_exp_f32_e32 v16, v16
	v_mul_f32_e32 v17, 0x4038aa3b, v17
	v_exp_f32_e32 v17, v17
	s_waitcnt lgkmcnt(1)
	v_mfma_f32_16x16x32_f16 v[26:29], v[34:37], v[70:73], v[26:29]
	v_rcp_f32_e32 v15, v15
	v_add_f32_e32 v16, 1.0, v16
	v_rcp_f32_e32 v16, v16
	v_add_f32_e32 v17, 1.0, v17
	v_rcp_f32_e32 v17, v17
	s_waitcnt lgkmcnt(0)
	v_mfma_f32_16x16x32_f16 v[26:29], v[30:33], v[74:77], v[26:29]
	v_fma_f32 v15, v15, -2.0, 1.0
	v_fmac_f32_e32 v14, v15, v93
	v_fma_f32 v15, v16, -2.0, 1.0
	v_add_f32_e32 v16, v24, v96
	s_waitcnt vmcnt(1)
	v_fmac_f32_e32 v14, v15, v98
	v_fma_f32 v15, v17, -2.0, 1.0
	v_mul_f32_e32 v16, 0x4038aa3b, v16
	v_add_f32_e32 v17, v25, v97
	v_exp_f32_e32 v16, v16
	v_mul_f32_e32 v17, 0x4038aa3b, v17
	v_add_f32_e32 v6, v26, v6
	v_exp_f32_e32 v17, v17
	v_mul_f32_e32 v6, 0x4038aa3b, v6
	v_exp_f32_e32 v6, v6
	v_fmac_f32_e32 v14, v15, v99
	v_add_f32_e32 v15, 1.0, v16
	v_rcp_f32_e32 v15, v15
	v_add_f32_e32 v16, 1.0, v17
	v_rcp_f32_e32 v16, v16
	v_add_f32_e32 v6, 1.0, v6
	v_rcp_f32_e32 v6, v6
	v_add_f32_e32 v7, v27, v7
	v_mul_f32_e32 v7, 0x4038aa3b, v7
	v_fma_f32 v15, v15, -2.0, 1.0
	v_exp_f32_e32 v7, v7
	v_fmac_f32_e32 v14, v15, v100
	v_fma_f32 v15, v16, -2.0, 1.0
	v_fmac_f32_e32 v14, v15, v101
	v_fma_f32 v6, v6, -2.0, 1.0
	s_waitcnt vmcnt(0)
	v_fmac_f32_e32 v14, v6, v2
	v_add_f32_e32 v6, v28, v8
	v_add_f32_e32 v2, 1.0, v7
	v_mul_f32_e32 v6, 0x4038aa3b, v6
	v_add_f32_e32 v7, v29, v9
	v_exp_f32_e32 v6, v6
	v_mul_f32_e32 v7, 0x4038aa3b, v7
	v_exp_f32_e32 v7, v7
	v_rcp_f32_e32 v2, v2
	v_add_f32_e32 v6, 1.0, v6
	v_rcp_f32_e32 v6, v6
	v_add_f32_e32 v7, 1.0, v7
	v_rcp_f32_e32 v7, v7
	v_fma_f32 v2, v2, -2.0, 1.0
	v_fmac_f32_e32 v14, v2, v3
	v_fma_f32 v2, v6, -2.0, 1.0
	v_fmac_f32_e32 v14, v2, v4
	v_fma_f32 v2, v7, -2.0, 1.0
	v_fmac_f32_e32 v14, v2, v5
	v_mov_b32_e32 v2, v14
	s_nop 1
	v_permlane16_swap_b32_e32 v14, v2
	v_add_f32_e32 v2, v14, v2
	v_mov_b32_e32 v3, v2
	s_nop 1
	v_permlane32_swap_b32_e32 v2, v3
	v_add_f32_e32 v2, v2, v3
	s_and_saveexec_b64 s[4:5], s[8:9]
	v_lshl_or_b32 v3, v11, 6, v0
	v_add_u32_e32 v3, 0x10000, v3
	ds_write_b32 v3, v2
	s_or_b64 exec, exec, s[4:5]
	v_cmp_eq_u32_e64 s[4:5], 0, v12
	s_and_b64 s[2:3], s[4:5], s[2:3]
	s_and_b64 s[2:3], s[2:3], vcc
	s_waitcnt lgkmcnt(0)
	s_barrier
	s_and_saveexec_b64 s[4:5], s[2:3]
	s_cbranch_execz .LBB1_4
	v_lshl_or_b32 v0, v11, 6, v0
	v_add_u32_e32 v0, 0x10000, v0
	ds_read_b32 v0, v0
	s_load_dwordx2 s[0:1], s[0:1], 0x30
	s_movk_i32 s2, 0xc8
	s_waitcnt lgkmcnt(0)
	v_add_f32_e32 v0, v2, v0
	v_add_f32_e32 v0, s6, v0
	v_mul_f32_e32 v0, 0xbfb8aa3b, v0
	v_exp_f32_e32 v0, v0
	s_nop 0
	v_add_f32_e32 v0, 1.0, v0
	v_rcp_f32_e32 v2, v0
	v_mad_u64_u32 v[0:1], s[2:3], v1, s2, v[10:11]
	v_ashrrev_i32_e32 v1, 31, v0
	v_lshl_add_u64 v[0:1], v[0:1], 2, s[0:1]
	global_store_dword v[0:1], v2, off
